# v79 + k1 role remap: virtual bid = bid with bits 5 and 7 swapped (chains on WG slots 0-3 and 16-19 of each XCD instead of 0-7)
# speedup vs baseline: 1.0144x; 1.0144x over previous
.LBB0_410:
	s_cmp_le_i32 s50, s2
	s_cselect_b64 s[4:5], -1, 0
	s_cmp_lt_i32 s2, s51
	s_cselect_b64 s[2:3], -1, 0
	s_and_b64 s[2:3], s[4:5], s[2:3]
	s_andn2_b64 vcc, exec, s[2:3]
	s_cbranch_vccnz .LBB0_789
	s_mov_b64 s[26:27], s[88:89]
	s_waitcnt lgkmcnt(0)
	s_load_dwordx8 s[4:11], s[26:27], 0x8
	s_load_dwordx2 s[74:75], s[26:27], 0x88
	v_mov_b32_e32 v196, v0
	s_mov_b32 s2, s87
	s_lshl_b32 s72, s33, 3
	s_lshl_b64 s[2:3], s[72:73], 2
	s_waitcnt lgkmcnt(0)
	s_add_u32 s66, s6, s2
	v_writelane_b32 v255, s4, 3
	s_addc_u32 s67, s7, s3
	s_mov_b32 s2, s87
	s_lshr_b32 s3, s87, 5
	s_lshr_b32 s12, s87, 7
	s_xor_b32 s3, s3, s12
	s_and_b32 s3, s3, 1
	s_mulk_i32 s3, 0xa0
	s_xor_b32 s2, s87, s3
	v_writelane_b32 v255, s5, 4
	v_writelane_b32 v255, s6, 5
	v_writelane_b32 v255, s7, 6
	v_writelane_b32 v255, s8, 7
	v_writelane_b32 v255, s9, 8
	v_writelane_b32 v255, s10, 9
	v_readfirstlane_b32 s12, v196
	v_writelane_b32 v255, s11, 10
	s_cmp_gt_i32 s2, 63
	s_mov_b64 s[34:35], -1
	s_cbranch_scc0 .LBB0_693
	s_load_dwordx4 s[4:7], s[26:27], 0x28
	s_ashr_i32 s3, s12, 6
	v_and_b32_e32 v224, 63, v196
	s_cmpk_gt_u32 s2, 0x7f
	s_waitcnt lgkmcnt(0)
	v_writelane_b32 v255, s4, 11
	s_nop 1
	v_writelane_b32 v255, s5, 12
	v_writelane_b32 v255, s6, 13
	v_writelane_b32 v255, s7, 14
	s_load_dwordx4 s[4:7], s[26:27], 0x58
	s_waitcnt lgkmcnt(0)
	v_writelane_b32 v255, s4, 15
	s_nop 1
	v_writelane_b32 v255, s5, 16
	v_writelane_b32 v255, s6, 17
	v_writelane_b32 v255, s7, 18
	s_load_dwordx2 s[4:5], s[26:27], 0x68
	s_mov_b64 s[26:27], -1
	s_waitcnt lgkmcnt(0)
	v_writelane_b32 v255, s4, 19
	s_nop 1
	v_writelane_b32 v255, s5, 20
	v_writelane_b32 v255, s3, 21
	s_cbranch_scc0 .LBB0_564
	s_add_i32 s3, s2, 0xffffff80
	s_cmp_eq_u32 s33, 0
	s_cselect_b32 s4, 0x50, 44
	s_mul_i32 s5, s3, s4
	s_movk_i32 s6, 0x2300
	v_writelane_b32 v255, s12, 25
	s_cselect_b32 s6, 0x4000, s6
	s_add_i32 s4, s5, s4
	s_min_u32 s4, s4, s6
	v_readlane_b32 s6, v255, 21
	s_add_i32 s7, s5, s6
	s_cmp_ge_i32 s7, s4
	s_cbranch_scc1 .LBB0_474
	s_add_i32 s8, s7, 0x1e00
	s_bitcmp0_b32 s33, 0
	s_mov_b32 s5, 0xc00000
	s_cselect_b32 s5, s5, 0x37a00000
	s_add_u32 s5, s74, s5
	s_addc_u32 s6, s75, 0
	s_cmpk_gt_i32 s7, 0xf7ff
	s_cbranch_scc0 .LBB0_428
	s_cmpk_gt_u32 s8, 0x19ff
	s_cbranch_scc0 .LBB0_425
	s_cmpk_gt_u32 s8, 0x1bff
	s_cbranch_scc0 .LBB0_422
	s_cmp_lt_u32 s7, 0xffffe200
	s_cbranch_scc0 .LBB0_419
	s_cmpk_gt_u32 s8, 0x3dff
	s_cselect_b64 s[10:11], -1, 0
	s_and_b64 s[12:13], s[10:11], exec
	s_movk_i32 s9, 0xc200
	s_cselect_b32 s9, s9, 0xffffe200
	s_add_i32 s9, s9, s8
	s_lshr_b32 s72, s9, 8
	s_bfe_u32 s12, s7, 0x40004
	s_lshl_b32 s13, s9, 5
	v_readlane_b32 s36, v255, 15
	s_and_b64 s[10:11], s[10:11], exec
	v_readlane_b32 s37, v255, 16
	v_readlane_b32 s38, v255, 17
	v_readlane_b32 s39, v255, 18
	s_cselect_b32 s14, 0x80, 0
	s_cselect_b32 s10, s39, s37
	s_cselect_b32 s11, s38, s36
	s_lshl_b32 s15, s33, 26
	s_add_u32 s15, s11, s15
	s_addc_u32 s26, s10, 0
	s_lshl_b64 s[10:11], s[72:73], 21
	s_add_u32 s10, s15, s10
	s_addc_u32 s11, s26, s11
	s_lshl_b32 s15, s12, 17
	s_add_u32 s10, s10, s15
	s_addc_u32 s11, s11, 0
	s_lshl_b32 s15, s9, 7
	s_and_b32 s15, s15, 0x780
	s_add_u32 s36, s10, s15
	s_addc_u32 s37, s11, 0
	s_lshl_b32 s9, s9, 6
	s_lshl_b32 s10, s72, 10
	s_and_b32 s9, s9, 0x300
	s_or_b32 s9, s9, s10
	s_or_b32 s9, s9, s14
	s_and_b32 s10, s13, 0x60
	s_or_b32 s72, s9, s10
	s_lshl_b64 s[10:11], s[72:73], 11
	s_add_u32 s9, s5, s10
	s_addc_u32 s10, s6, s11
	s_lshl_b32 s11, s12, 7
	s_add_u32 s9, s9, s11
	s_addc_u32 s10, s10, 0
	s_add_u32 s38, s9, 0x1e00000
	s_addc_u32 s39, s10, 0
	s_mov_b64 s[26:27], 0
